# adds phase-prologue de-serialisation: PEER and LN vector-cache fills and attention rope-table copy issue all loads before writing LDS
# baseline (speedup 1.0000x reference)
.LBB0_307:
	s_or_saveexec_b64 s[8:9], s[8:9]
	v_mov_b64_e32 v[6:7], s[40:41]
	s_xor_b64 exec, exec, s[8:9]
	s_add_u32 s4, s4, 0x2000
	s_addc_u32 s5, s5, 0
	v_mov_b64_e32 v[6:7], s[4:5]
	s_or_b64 exec, exec, s[8:9]
	v_lshl_add_u64 v[6:7], v[6:7], 0, v[2:3]
	global_load_dwordx4 v[10:13], v[6:7], off
	s_movk_i32 s4, 0xc00
	v_cmp_gt_i32_e32 vcc, s4, v9
	s_waitcnt vmcnt(0)
	ds_write_b128 v5, v[10:13] offset:8192
	s_and_saveexec_b64 s[4:5], vcc
	s_cbranch_execz .LBB0_312
	s_load_dwordx2 s[8:9], s[0:1], 0xa8
	v_lshlrev_b32_e32 v2, 4, v9
	s_mov_b64 s[40:41], 0
	v_mov_b32_e32 v6, v9
	s_waitcnt lgkmcnt(0)
	s_add_u32 s8, s8, 0x200000
	s_addc_u32 s9, s9, 0
	v_lshrrev_b32_e32 v5, 4, v6
	v_and_b32_e32 v7, 0xf0, v2
	v_mul_lo_u32 v5, v5, s95
	v_add3_u32 v5, s31, v5, v7
	global_load_dwordx4 v[222:225], v2, s[8:9]
	v_add_u32_e32 v10, 0x2000, v2
	global_load_dwordx4 v[226:229], v10, s[8:9]
	v_add_u32_e32 v11, 0x4000, v2
	global_load_dwordx4 v[230:233], v11, s[8:9]
	v_add_u32_e32 v12, 0x6000, v2
	global_load_dwordx4 v[234:237], v12, s[8:9]
	v_add_u32_e32 v13, 0x8000, v2
	global_load_dwordx4 v[238:241], v13, s[8:9]
	v_add_u32_e32 v14, 0xa000, v2
	global_load_dwordx4 v[242:245], v14, s[8:9]
	s_waitcnt vmcnt(5)
	ds_write_b128 v5, v[222:225]
	s_waitcnt vmcnt(4)
	ds_write_b128 v5, v[226:229] offset:8704
	s_waitcnt vmcnt(3)
	ds_write_b128 v5, v[230:233] offset:17408
	s_waitcnt vmcnt(2)
	ds_write_b128 v5, v[234:237] offset:26112
	s_waitcnt vmcnt(1)
	ds_write_b128 v5, v[238:241] offset:34816
	s_waitcnt vmcnt(0)
	ds_write_b128 v5, v[242:245] offset:43520

.LBB0_512:
	s_load_dwordx4 s[44:47], s[0:1], 0x60
	v_lshlrev_b32_e32 v5, 6, v8
	v_bfe_u32 v4, v8, 1, 6
	v_and_b32_e32 v5, 64, v5
	v_and_b32_e32 v6, 0xfffff80, v8
	v_or3_b32 v4, v6, v5, v4
	v_lshlrev_b32_e32 v12, 4, v4
	v_lshlrev_b32_e32 v10, 4, v8
	s_lshl_b32 s6, s36, 11
	s_lshl_b64 s[8:9], s[6:7], 2
	s_waitcnt lgkmcnt(0)
	s_add_u32 s40, s44, s8
	s_addc_u32 s41, s45, s9
	global_load_dwordx4 v[24:27], v10, s[40:41]
	s_add_u32 s8, s46, s8
	s_addc_u32 s9, s47, s9
	global_load_dwordx4 v[28:31], v10, s[8:9]
	s_add_u32 s6, s4, 0x100000
	s_addc_u32 s8, s5, 0
	s_mul_i32 s37, s36, 3
	s_add_i32 s27, s37, 0
	s_mul_i32 s27, s27, 0xc000
	s_add_i32 s27, s27, 0x6000
	s_add_u32 s40, s6, s27
	s_addc_u32 s41, s8, 0
	global_load_dwordx4 v[32:35], v10, s[40:41]
	s_add_i32 s27, s37, 1
	s_mul_i32 s27, s27, 0xc000
	s_add_i32 s27, s27, 0x6000
	s_add_u32 s40, s6, s27
	s_addc_u32 s41, s8, 0
	global_load_dwordx4 v[36:39], v10, s[40:41]
	s_add_i32 s27, s37, 2
	s_mul_i32 s27, s27, 0xc000
	s_add_i32 s27, s27, 0x6000
	s_add_u32 s40, s6, s27
	s_addc_u32 s41, s8, 0
	global_load_dwordx4 v[40:43], v10, s[40:41]
	s_add_i32 s27, s37, 0
	s_mul_i32 s27, s27, 0xc000
	s_add_i32 s27, s27, 0x8000
	s_add_u32 s40, s6, s27
	s_addc_u32 s41, s8, 0
	global_load_dwordx4 v[44:47], v10, s[40:41]
	s_add_i32 s27, s37, 1
	s_mul_i32 s27, s27, 0xc000
	s_add_i32 s27, s27, 0x8000
	s_add_u32 s40, s6, s27
	s_addc_u32 s41, s8, 0
	global_load_dwordx4 v[48:51], v10, s[40:41]
	s_add_i32 s27, s37, 2
	s_mul_i32 s27, s27, 0xc000
	s_add_i32 s27, s27, 0x8000
	s_add_u32 s40, s6, s27
	s_addc_u32 s41, s8, 0
	global_load_dwordx4 v[52:55], v10, s[40:41]
	s_add_i32 s27, s37, 0
	s_mul_i32 s27, s27, 0xc000
	s_add_i32 s27, s27, 0x4000
	s_add_u32 s40, s6, s27
	s_addc_u32 s41, s8, 0
	global_load_dwordx4 v[56:59], v10, s[40:41]
	s_add_i32 s27, s37, 1
	s_mul_i32 s27, s27, 0xc000
	s_add_i32 s27, s27, 0x4000
	s_add_u32 s40, s6, s27
	s_addc_u32 s41, s8, 0
	global_load_dwordx4 v[60:63], v10, s[40:41]
	s_add_i32 s27, s37, 2
	s_mul_i32 s27, s27, 0xc000
	s_add_i32 s27, s27, 0x4000
	s_add_u32 s40, s6, s27
	s_addc_u32 s41, s8, 0
	global_load_dwordx4 v[64:67], v10, s[40:41]
	v_add_u32_e32 v13, 0x4000, v12
	v_add_u32_e32 v14, 0xc000, v12
	s_waitcnt vmcnt(10)
	ds_write_b128 v12, v[24:27]
	s_waitcnt vmcnt(9)
	ds_write_b128 v12, v[28:31] offset:8192
	s_waitcnt vmcnt(8)
	ds_write_b128 v13, v[32:35]
	s_waitcnt vmcnt(7)
	ds_write_b128 v13, v[36:39] offset:8192
	s_waitcnt vmcnt(6)
	ds_write_b128 v13, v[40:43] offset:16384
	s_waitcnt vmcnt(5)
	ds_write_b128 v13, v[44:47] offset:24576
	s_waitcnt vmcnt(4)
	ds_write_b128 v14, v[48:51]
	s_waitcnt vmcnt(3)
	ds_write_b128 v14, v[52:55] offset:8192
	s_waitcnt vmcnt(2)
	ds_write_b128 v14, v[56:59] offset:16384
	s_waitcnt vmcnt(1)
	ds_write_b128 v14, v[60:63] offset:24576
	s_waitcnt vmcnt(0)
	ds_write_b128 v14, v[64:67] offset:32768
	s_andn2_b64 vcc, exec, s[42:43]
	s_waitcnt lgkmcnt(0)
	s_barrier
	s_cbranch_vccnz .LBB0_545
	v_add_u32_e32 v145, 0, v2
	ds_read_b128 v[4:7], v145
	ds_read_b128 v[8:11], v145 offset:1024
	ds_read_b128 v[12:15], v145 offset:8192
	ds_read_b128 v[16:19], v145 offset:9216
	ds_read_b128 v[20:23], v145 offset:2048
	ds_read_b128 v[24:27], v145 offset:3072
	ds_read_b128 v[28:31], v145 offset:10240
	ds_read_b128 v[32:35], v145 offset:11264
	ds_read_b128 v[36:39], v145 offset:4096
	ds_read_b128 v[40:43], v145 offset:5120
	ds_read_b128 v[44:47], v145 offset:12288
	ds_read_b128 v[48:51], v145 offset:13312
	ds_read_b128 v[52:55], v145 offset:6144
	ds_read_b128 v[56:59], v145 offset:7168
	ds_read_b128 v[60:63], v145 offset:14336
	ds_read_b128 v[64:67], v145 offset:15360
	s_cmp_lg_u32 s36, 0
	s_cselect_b64 s[44:45], -1, 0
	s_add_u32 s27, s0, 16
	s_addc_u32 s37, s1, 0
	s_ashr_i32 s53, s52, 31
	s_lshl_b64 s[8:9], s[52:53], 2
	s_add_u32 s56, s8, 0x3d200000
	s_addc_u32 s57, s9, 0
	s_lshl_b64 s[8:9], s[52:53], 11
	v_or_b32_e32 v146, s8, v144
	v_mov_b32_e32 v147, s9
	v_lshl_or_b32 v148, v68, 2, s8
	v_mov_b32_e32 v149, s9
	s_lshl_b64 s[8:9], s[52:53], 12
	v_readlane_b32 s6, v253, 11
	v_or_b32_e32 v150, s8, v2
	s_add_i32 s8, s6, s50
	v_mov_b32_e32 v151, s9
	s_ashr_i32 s9, s8, 31
	s_lshl_b64 s[42:43], s[8:9], 12
	s_lshl_b64 s[8:9], s[8:9], 11
	v_cmp_eq_u32_e64 s[40:41], 0, v68
	s_lshl_b64 s[46:47], s[52:53], 13
	v_or_b32_e32 v152, s42, v2
	v_mov_b32_e32 v153, s43
	v_or_b32_e32 v154, s8, v144
	v_mov_b32_e32 v155, s9
	s_and_b64 vcc, exec, s[44:45]
	s_cbranch_vccnz .Lln0_pre_done
	v_lshlrev_b32_e32 v228, 2, v144
	s_add_i32 s6, s52, 0xffffc000
	s_lshl_b64 s[42:43], s[6:7], 13
	s_cmpk_lt_i32 s52, 0x4000
	s_cselect_b32 s9, s1, s37
	s_cselect_b32 s8, s0, s27
	s_cselect_b32 s100, s46, s42
	s_cselect_b32 s101, s47, s43
	s_load_dwordx2 s[8:9], s[8:9], 0x0
	s_waitcnt lgkmcnt(0)
	s_add_u32 s8, s8, s100
	s_addc_u32 s9, s9, s101
	global_load_dwordx4 v[182:185], v228, s[8:9] offset:16
	global_load_dwordx4 v[186:189], v228, s[8:9]
	global_load_dwordx4 v[190:193], v228, s[8:9] offset:2064
	global_load_dwordx4 v[194:197], v228, s[8:9] offset:2048
	s_add_u32 s8, s8, 0x1000
	s_addc_u32 s9, s9, 0
	global_load_dwordx4 v[198:201], v228, s[8:9]
	global_load_dwordx4 v[202:205], v228, s[8:9] offset:16
	global_load_dwordx4 v[220:223], v228, s[8:9] offset:2048
	global_load_dwordx4 v[224:227], v228, s[8:9] offset:2064

.LBB0_708:
	s_or_b64 exec, exec, s[4:5]
	s_load_dwordx2 s[50:51], s[0:1], 0xa8
	s_waitcnt vmcnt(0)
	v_lshlrev_b32_e32 v5, 6, v2
	v_lshrrev_b32_e32 v4, 3, v2
	v_and_b32_e32 v5, 0x1c0, v5
	s_cmp_lg_u32 s36, 3
	v_add_lshl_u32 v6, v5, v4, 4
	s_cselect_b64 s[96:97], -1, 0
	v_lshlrev_b32_e32 v4, 2, v2
	s_waitcnt lgkmcnt(0)
	s_add_u32 s4, s50, 0x100000
	v_readlane_b32 s6, v253, 15
	v_ashrrev_i32_e32 v5, 31, v4
	s_addc_u32 s5, s51, 0
	v_add_u32_e32 v7, s6, v6
	s_load_dwordx4 s[40:43], s[0:1], 0x90
	v_lshlrev_b32_e32 v8, 4, v2
	s_cmp_lg_u32 s36, 3
	s_cselect_b32 s9, 1, 0
	s_add_i32 s9, s36, s9
	s_mul_i32 s8, s36, 3
	s_mul_i32 s9, s9, 3
	s_add_i32 s37, s8, 0
	s_mul_i32 s37, s37, 0xc000
	s_add_i32 s37, s37, 0xa000
	s_add_u32 s52, s4, s37
	s_addc_u32 s53, s5, 0
	global_load_dwordx4 v[24:27], v8, s[52:53]
	s_add_i32 s37, s8, 1
	s_mul_i32 s37, s37, 0xc000
	s_add_i32 s37, s37, 0xa000
	s_add_u32 s52, s4, s37
	s_addc_u32 s53, s5, 0
	global_load_dwordx4 v[28:31], v8, s[52:53]
	s_add_i32 s37, s8, 2
	s_mul_i32 s37, s37, 0xc000
	s_add_i32 s37, s37, 0xa000
	s_add_u32 s52, s4, s37
	s_addc_u32 s53, s5, 0
	global_load_dwordx4 v[32:35], v8, s[52:53]
	s_add_i32 s37, s9, 0
	s_mul_i32 s37, s37, 0xc000
	s_add_u32 s52, s4, s37
	s_addc_u32 s53, s5, 0
	global_load_dwordx4 v[36:39], v8, s[52:53]
	s_add_i32 s37, s9, 1
	s_mul_i32 s37, s37, 0xc000
	s_add_u32 s52, s4, s37
	s_addc_u32 s53, s5, 0
	global_load_dwordx4 v[40:43], v8, s[52:53]
	s_add_i32 s37, s9, 2
	s_mul_i32 s37, s37, 0xc000
	s_add_u32 s52, s4, s37
	s_addc_u32 s53, s5, 0
	global_load_dwordx4 v[44:47], v8, s[52:53]
	s_add_i32 s37, s9, 0
	s_mul_i32 s37, s37, 0xc000
	s_add_i32 s37, s37, 0x2000
	s_add_u32 s52, s4, s37
	s_addc_u32 s53, s5, 0
	global_load_dwordx4 v[48:51], v8, s[52:53]
	s_add_i32 s37, s9, 1
	s_mul_i32 s37, s37, 0xc000
	s_add_i32 s37, s37, 0x2000
	s_add_u32 s52, s4, s37
	s_addc_u32 s53, s5, 0
	global_load_dwordx4 v[52:55], v8, s[52:53]
	s_add_i32 s37, s9, 2
	s_mul_i32 s37, s37, 0xc000
	s_add_i32 s37, s37, 0x2000
	s_add_u32 s52, s4, s37
	s_addc_u32 s53, s5, 0
	global_load_dwordx4 v[56:59], v8, s[52:53]
	s_waitcnt lgkmcnt(0)
	s_lshl_b32 s6, s36, 11
	s_lshl_b64 s[4:5], s[6:7], 2
	s_add_u32 s8, s40, s4
	s_addc_u32 s9, s41, s5
	global_load_dwordx4 v[60:63], v8, s[8:9]
	s_add_u32 s4, s42, s4
	s_addc_u32 s5, s43, s5
	global_load_dwordx4 v[64:67], v8, s[4:5]
	s_lshl_b32 s6, s36, 6
	v_and_b32_e32 v21, 63, v2
	v_cmp_eq_u32_e64 s[40:41], 0, v21
	s_lshl_b64 s[4:5], s[6:7], 2
	v_readlane_b32 s6, v254, 50
	s_add_u32 s66, s6, s4
	v_readlane_b32 s4, v254, 51
	s_addc_u32 s67, s4, s5
	v_add_u32_e32 v9, 0x8000, v7
	v_add_u32_e32 v11, 0x1c200, v6
	v_add_u32_e32 v12, 0x1e200, v6
	s_waitcnt vmcnt(10)
	ds_write_b128 v7, v[24:27]
	s_waitcnt vmcnt(9)
	ds_write_b128 v7, v[28:31] offset:8192
	s_waitcnt vmcnt(8)
	ds_write_b128 v7, v[32:35] offset:16384
	s_waitcnt vmcnt(7)
	ds_write_b128 v7, v[36:39] offset:24576
	s_waitcnt vmcnt(6)
	ds_write_b128 v9, v[40:43]
	s_waitcnt vmcnt(5)
	ds_write_b128 v9, v[44:47] offset:8192
	s_waitcnt vmcnt(4)
	ds_write_b128 v9, v[48:51] offset:16384
	s_waitcnt vmcnt(3)
	ds_write_b128 v9, v[52:55] offset:24576
	s_waitcnt vmcnt(2)
	ds_write_b128 v9, v[56:59] offset:32768
	s_waitcnt vmcnt(1)
	ds_write_b128 v11, v[60:63]
	s_waitcnt vmcnt(0)
	ds_write_b128 v12, v[64:67]
	v_mov_b32_e32 v4, 0
	s_waitcnt lgkmcnt(0)
	s_barrier
	v_readlane_b32 s6, v254, 3
	s_lshr_b32 s4, s27, 6
	s_add_i32 s6, s6, s4
	v_readlane_b32 s44, v253, 31
	v_readlane_b32 s45, v253, 32
	s_mov_b32 s88, s6
	s_cmp_lt_i32 s88, s26
	v_lshlrev_b32_e32 v20, 6, v21
	s_cselect_b64 s[4:5], -1, 0
	s_cmp_ge_i32 s88, s26
	v_and_b32_e32 v24, 0xf00, v20
	v_and_b32_e32 v22, 0xc0, v20
	s_cbranch_scc1 .LBB0_716
	s_ashr_i32 s89, s88, 31
	s_lshl_b64 s[8:9], s[88:89], 12
	s_add_u32 s8, s50, s8
	s_addc_u32 s9, s51, s9
	v_mov_b32_e32 v25, v3
	v_lshl_add_u64 v[4:5], s[8:9], 0, v[24:25]
	v_mov_b32_e32 v23, v3
	v_lshl_add_u64 v[4:5], v[4:5], 0, v[22:23]
	s_mov_b64 s[8:9], 0x24d00000
	s_mov_b32 s6, 0x24d00000
	v_lshl_add_u64 v[16:17], v[4:5], 0, s[8:9]
	v_add_co_u32_e32 v4, vcc, s6, v4
	s_nop 1
	v_addc_co_u32_e32 v5, vcc, 0, v5, vcc
	global_load_dwordx4 v[4:7], v[4:5], off
	s_nop 0
	global_load_dwordx4 v[8:11], v[16:17], off offset:48
	global_load_dwordx4 v[12:15], v[16:17], off offset:32
	s_nop 0
	global_load_dwordx4 v[16:19], v[16:17], off offset:16
